# v039 + diff MFMA segment regenerated: rows-0..31 QK chain first with K fragments prefetched before the barrier, persistent seed tuple, next addresses at M end
# speedup vs baseline: 1.0256x; 1.0256x over previous
; #define SBAR() __builtin_amdgcn_sched_barrier(0)
; __device__ __forceinline__ int kg(int row) { return (row >> 1) & 7; }
; __device__ __forceinline__ int v_rd_base(int lane) { return ((lane & 3) << 3) | (((lane >> 2) & 3) << 6) | (((lane >> 4) & 1) << 5) | (((lane >> 5) & 1) << 8); }
; #define BAR_ALL() asm volatile("s_waitcnt lgkmcnt(0)\n\ts_barrier" ::: "memory")
; #define LWN1(a) do { if constexpr (NW == 0) LW1(0, a); else if constexpr (NW == 1) LW1(1, a); else if constexpr (NW == 2) LW1(2, a); else if constexpr (NW == 3) LW1(3, a); else if constexpr (NW == 4) LW1(4, a); else if constexpr (NW == 5) LW1(5, a); else LW1(6, a); } while (0)
; #define DMA_K(tile, b) DMA_KP(Kh, tile, b)
; #define DMA_V(tile, b) DMA_VP(Vh, tile, b)
; template <int DQK, bool HASQK, bool HASPV, int J> ...
;     ...
;     if constexpr (J < NS) {
;         constexpr int rd1 = (J + 1 < NS) ? ((J + 1 < NQS) ? 1 : 2) : 0, rd2 = (J + 2 < NS) ? ((J + 2 < NQS) ? 1 : 2) : 0, rd3 = (J + 3 < NS) ? ((J + 3 < NQS) ? 1 : 2) : 0, NW = rd1 + rd2 + rd3;
;     ...
;         if constexpr (J < NQS) { constexpr int d0 = J >> 1, h = J & 1;
;             LWN1(kf[d0][h]); SBAR();
;             if constexpr (h == 0) p0 = __builtin_amdgcn_mfma_f32_32x32x16_bf16(kf[d0][0], qr[d0], (d0 == 0) ? negm : p0, 0, 0, 0);
;             else p1 = __builtin_amdgcn_mfma_f32_32x32x16_bf16(kf[d0][1], qr[d0], (d0 == 0) ? negm : p1, 0, 0, 0);
;         } else { constexpr int q = J - NQS, g = q >> 2, d = q & 3;
;             LWN2(vf[g][2 * d], vf[g][2 * d + 1]); SBAR();
;             o[d] = __builtin_amdgcn_mfma_f32_32x32x16_bf16(pa[g], (bf16x8){vf[g][2 * d][0], vf[g][2 * d][1], vf[g][2 * d][2], vf[g][2 * d][3], vf[g][2 * d + 1][0], vf[g][2 * d + 1][1], vf[g][2 * d + 1][2], vf[g][2 * d + 1][3]}, o[d], 0, 0, 0);
;         }
;     ...
;     const int vb0 = (int)(uintptr_t)V_lds + v_rd_base(lane);
;     int ka[4];
; #pragma unroll
;     for (int b = 0; b < 4; ++b) ka[b] = (int)(uintptr_t)lds + r32 * RB + ((b * 32 + hi * 16) ^ (kg(r32) << 4));
;     f32x16 p0, p1; bf16x8 pa0, pa1, pa2, pa3;
;     asm volatile("s_waitcnt vmcnt(0)" ::: "memory"); BAR_ALL();
;     if (ATT_SKEW && g == 1) BAR_ALL();
;     ...
;     int ci = 0;
;     if (DMA_M) { DMA_K(2, 2); DMA_V(1, 1); }
;     SEG_M(true, false, 0, 0); BAR_ALL();
.LBB0_648:
	v_lshlrev_b32_e32 v26, 3, v156
	v_and_b32_e32 v23, 0xc0, v23
	s_cmp_lg_u32 0, -1
	v_and_or_b32 v23, v26, 24, v23
	v_and_b32_e32 v24, 32, v24
	v_and_b32_e32 v27, 0x100, v26
	s_cselect_b32 s10, 0, 0
	v_lshlrev_b32_e32 v154, 4, v25
	v_or3_b32 v23, v23, v24, v27
	v_lshl_add_u32 v24, v22, 7, s10
	v_and_b32_e32 v25, 0x70, v26
	v_add_u32_e32 v26, 32, v154
	v_xad_u32 v143, v26, v25, v24
	v_add_u32_e32 v26, 64, v154
	v_xad_u32 v160, v26, v25, v24
	v_add_u32_e32 v26, 0x60, v154
	v_xad_u32 v141, v154, v25, v24
	v_xad_u32 v161, v26, v25, v24
	s_addk_i32 s10, 0x6000
	ds_read_b128 v[24:27], v141 offset:0
	ds_read_b128 v[28:31], v141 offset:0x1000
	ds_read_b128 v[32:35], v143 offset:0
	ds_read_b128 v[36:39], v143 offset:0x1000
	v_add_u32_e32 v157, s10, v23
	v_cndmask_b32_e64 v23, 0, 1, s[26:27]
	s_mov_b32 s86, 0
	v_lshlrev_b32_e32 v23, 7, v23
	v_mov_b64_e32 v[94:95], v[14:15]
	v_mov_b64_e32 v[92:93], v[12:13]
	v_mov_b64_e32 v[90:91], v[10:11]
	v_mov_b64_e32 v[88:89], v[8:9]
	v_mov_b64_e32 v[86:87], v[6:7]
	v_mov_b64_e32 v[84:85], v[4:5]
	v_mov_b64_e32 v[82:83], v[2:3]
	v_mov_b64_e32 v[80:81], v[0:1]
	s_waitcnt lgkmcnt(3)
	s_waitcnt vmcnt(0)
	s_nop 0
	v_mfma_f32_32x32x16_bf16 v[96:111], v[24:27], v[112:115], v[80:95]
	ds_read_b128 v[24:27], v160 offset:0
	s_waitcnt lgkmcnt(3)
	s_nop 0
	v_mfma_f32_32x32x16_bf16 v[80:95], v[28:31], v[112:115], v[80:95]
	ds_read_b128 v[28:31], v160 offset:0x1000
	s_waitcnt lgkmcnt(3)
	s_nop 0
	v_mfma_f32_32x32x16_bf16 v[96:111], v[32:35], v[116:119], v[96:111]
	ds_read_b128 v[32:35], v161 offset:0
	s_waitcnt lgkmcnt(3)
	s_nop 0
	v_mfma_f32_32x32x16_bf16 v[80:95], v[36:39], v[116:119], v[80:95]
	ds_read_b128 v[36:39], v161 offset:0x1000
	s_waitcnt lgkmcnt(3)
	s_nop 0
	v_mfma_f32_32x32x16_bf16 v[96:111], v[24:27], v[120:123], v[96:111]
	s_waitcnt lgkmcnt(2)
	s_nop 0
	v_mfma_f32_32x32x16_bf16 v[80:95], v[28:31], v[120:123], v[80:95]
	s_waitcnt lgkmcnt(1)
	s_nop 0
	v_mfma_f32_32x32x16_bf16 v[96:111], v[32:35], v[124:127], v[96:111]
	s_waitcnt lgkmcnt(0)
	s_nop 0
	v_mfma_f32_32x32x16_bf16 v[80:95], v[36:39], v[124:127], v[80:95]
	s_and_b32 s46, s46, 3
	s_lshl_b64 s[44:45], s[44:45], 23
	s_lshl_b32 s46, s46, 8
	v_lshlrev_b32_e32 v20, 2, v20
	v_lshlrev_b32_e32 v17, 2, v17
	s_or_b32 s44, s44, s46
	v_and_b32_e32 v20, 0xffffe000, v20
	v_lshlrev_b32_e32 v18, 10, v18
	v_and_b32_e32 v17, 0xffffe000, v17
	v_lshl_add_u32 v155, v22, 2, s67
	v_or_b32_e32 v22, s44, v23
	v_mov_b32_e32 v23, s45
	v_or3_b32 v20, v20, v18, v21
	s_add_u32 s44, s73, s44
	v_or3_b32 v17, v17, v18, v19
	s_waitcnt lgkmcnt(0)
	s_barrier
	v_lshl_add_u64 v[22:23], s[24:25], 0, v[22:23]
	v_add_u32_e32 v20, v20, v16
	v_mov_b32_e32 v21, v139
	s_addc_u32 s45, s74, s45
	v_add_u32_e32 v16, v17, v16
	v_mov_b32_e32 v17, v139
	v_mov_b32_e32 v64, v139
	v_mov_b32_e32 v65, v139
	v_lshl_add_u64 v[144:145], v[22:23], 0, v[138:139]
	v_lshl_add_u64 v[146:147], s[44:45], 0, v[20:21]
	v_lshl_add_u64 v[148:149], s[44:45], 0, v[16:17]
	v_mov_b32_e32 v66, v139
	v_mov_b32_e32 v67, v139
	v_mov_b32_e32 v68, v139
	v_mov_b32_e32 v69, v139
	v_mov_b32_e32 v70, v139
	v_mov_b32_e32 v71, v139
	v_mov_b32_e32 v72, v139
	v_mov_b32_e32 v73, v139
	v_mov_b32_e32 v74, v139
	v_mov_b32_e32 v75, v139
	v_mov_b32_e32 v76, v139
	v_mov_b32_e32 v77, v139
	v_mov_b32_e32 v78, v139
	v_mov_b32_e32 v79, v139
	v_mov_b64_e32 v[48:49], v[64:65]
	v_mov_b64_e32 v[32:33], v[64:65]
	v_mov_b64_e32 v[16:17], v[64:65]
	v_cmp_gt_u32_e64 s[10:11], 32, v156
	v_mov_b32_e32 v159, 0
	s_mov_b64 s[44:45], 0
	v_mov_b64_e32 v[50:51], v[66:67]
	v_mov_b64_e32 v[52:53], v[68:69]
	v_mov_b64_e32 v[54:55], v[70:71]
	v_mov_b64_e32 v[56:57], v[72:73]
	v_mov_b64_e32 v[58:59], v[74:75]
	v_mov_b64_e32 v[60:61], v[76:77]
	v_mov_b64_e32 v[62:63], v[78:79]
	v_mov_b64_e32 v[34:35], v[66:67]
	v_mov_b64_e32 v[36:37], v[68:69]
	v_mov_b64_e32 v[38:39], v[70:71]
	v_mov_b64_e32 v[40:41], v[72:73]
	v_mov_b64_e32 v[42:43], v[74:75]
	v_mov_b64_e32 v[44:45], v[76:77]
	v_mov_b64_e32 v[46:47], v[78:79]
	v_mov_b64_e32 v[18:19], v[66:67]
	v_mov_b64_e32 v[20:21], v[68:69]
	v_mov_b64_e32 v[22:23], v[70:71]
	v_mov_b64_e32 v[24:25], v[72:73]
	v_mov_b64_e32 v[26:27], v[74:75]
	v_mov_b64_e32 v[28:29], v[76:77]
	v_mov_b64_e32 v[30:31], v[78:79]
	v_mov_b32_e32 v158, 0
	s_add_i32 s46, s86, 1
	s_cmp_lg_u32 s86, 2
	s_cselect_b32 s46, s46, 0
	s_lshl_b32 s47, s46, 13
	s_lshl_b32 s46, s86, 14
	v_add_u32_e32 v188, s46, v157
	v_add_u32_e32 v232, s47, v141
	v_add_u32_e32 v233, s47, v143
	v_add_u32_e32 v186, s47, v160
	v_add_u32_e32 v187, s47, v161
	s_branch .LBB0_652

; __device__ __forceinline__ int crow(int r, int hi) { return (r & 3) + 8 * (r >> 2) + 4 * hi; }
; #define PK4(P, BASE, OUT) do { u32x4 w = {cvtpk(P[BASE + 0], P[BASE + 1]), cvtpk(P[BASE + 2], P[BASE + 3]), cvtpk(P[BASE + 4], P[BASE + 5]), cvtpk(P[BASE + 6], P[BASE + 7])}; \
;     OUT = *reinterpret_cast<bf16x8*>(&w); } while (0)
; __device__ __forceinline__ void smax_tile(f32x16& p0, f32x16& p1, float& mhat, float& l_reg, f32x16 (&o)[4], float* al_l, const bool first, int r32, int hi,
;                                           bf16x8& pa0, bf16x8& pa1, bf16x8& pa2, bf16x8& pa3) {
;     ...
;         const float dl = first ? rm : fmaxf(rm, 0.f);
;         mhat += dl;
; #pragma unroll
;         for (int r = 0; r < 16; ++r) { p0[r] -= dl; p1[r] -= dl; }
;         if (!first) { const float f = __builtin_amdgcn_exp2f(-dl); l_reg *= f;
;             if (hi == 0) al_l[r32] = f; asm volatile("s_waitcnt lgkmcnt(0)" ::: "memory");
; #pragma unroll
;             for (int d = 0; d < 4; ++d)
; #pragma unroll
;                 for (int r = 0; r < 16; ++r) o[d][r] *= al_l[crow(r, hi)]; }
;     }
; #pragma unroll
;     for (int r = 0; r < 16; ++r) p0[r] = __builtin_amdgcn_exp2f(p0[r]);
; #pragma unroll
;     for (int r = 0; r < 16; ++r) p1[r] = __builtin_amdgcn_exp2f(p1[r]);
;     float ps = p0[0];
; #pragma unroll
;     for (int r = 1; r < 16; ++r) ps += p0[r];
; #pragma unroll
;     for (int r = 0; r < 16; ++r) ps += p1[r];
;     { auto rr = __builtin_amdgcn_permlane32_swap(__float_as_uint(ps), __float_as_uint(ps), false, false); ps = __uint_as_float(rr[0]) + __uint_as_float(rr[1]); }
;     l_reg += ps;
;     ...
;     PK4(p0, 0, pa0); PK4(p0, 8, pa1); PK4(p1, 0, pa2); PK4(p1, 8, pa3);
.LBB0_650:
	v_add_f32_e32 v158, v158, v128
	v_xor_b32_e32 v200, 0x80000000, v158
	v_mov_b32_e32 v201, v200
	v_mov_b32_e32 v202, v200
	v_mov_b32_e32 v203, v200
	v_mov_b32_e32 v204, v200
	v_mov_b32_e32 v205, v200
	v_mov_b32_e32 v206, v200
	v_mov_b32_e32 v207, v200
	v_mov_b32_e32 v208, v200
	v_mov_b32_e32 v209, v200
	v_mov_b32_e32 v210, v200
	v_mov_b32_e32 v211, v200
	v_mov_b32_e32 v212, v200
	v_mov_b32_e32 v213, v200
	v_mov_b32_e32 v214, v200
	v_mov_b32_e32 v215, v200
	v_sub_f32_e32 v111, v111, v128
	v_sub_f32_e32 v110, v110, v128
	v_sub_f32_e32 v109, v109, v128
	v_sub_f32_e32 v108, v108, v128
	v_sub_f32_e32 v107, v107, v128
	v_sub_f32_e32 v106, v106, v128
	v_sub_f32_e32 v105, v105, v128
	v_sub_f32_e32 v104, v104, v128
	v_sub_f32_e32 v103, v103, v128
	v_sub_f32_e32 v102, v102, v128
	v_sub_f32_e32 v101, v101, v128
	v_sub_f32_e32 v100, v100, v128
	v_sub_f32_e32 v99, v99, v128
	v_sub_f32_e32 v98, v98, v128
	v_sub_f32_e32 v97, v97, v128
	v_sub_f32_e32 v96, v96, v128
	v_sub_f32_e32 v95, v95, v128
	v_sub_f32_e32 v94, v94, v128
	v_sub_f32_e32 v93, v93, v128
	v_sub_f32_e32 v92, v92, v128
	v_sub_f32_e32 v91, v91, v128
	v_sub_f32_e32 v90, v90, v128
	v_sub_f32_e32 v89, v89, v128
	v_sub_f32_e32 v88, v88, v128
	v_sub_f32_e32 v87, v87, v128
	v_sub_f32_e32 v86, v86, v128
	v_sub_f32_e32 v85, v85, v128
	v_sub_f32_e32 v84, v84, v128
	v_sub_f32_e32 v83, v83, v128
	v_sub_f32_e32 v82, v82, v128
	v_sub_f32_e32 v81, v81, v128
	v_sub_f32_e32 v80, v80, v128
.LBB0_651:
	v_exp_f32_e32 v96, v96
	v_exp_f32_e32 v97, v97
	v_exp_f32_e32 v98, v98
	v_exp_f32_e32 v99, v99
	v_exp_f32_e32 v100, v100
	v_exp_f32_e32 v101, v101
	v_add_f32_e32 v128, v96, v97
	v_exp_f32_e32 v102, v102
	v_add_f32_e32 v128, v98, v128
	v_exp_f32_e32 v103, v103
	v_add_f32_e32 v128, v99, v128
	v_exp_f32_e32 v104, v104
	v_add_f32_e32 v128, v100, v128
	v_exp_f32_e32 v105, v105
	v_add_f32_e32 v128, v101, v128
	v_exp_f32_e32 v106, v106
	v_add_f32_e32 v128, v102, v128
	v_exp_f32_e32 v107, v107
	v_add_f32_e32 v128, v103, v128
	v_exp_f32_e32 v108, v108
	v_add_f32_e32 v128, v104, v128
	v_exp_f32_e32 v109, v109
	v_add_f32_e32 v128, v105, v128
	v_exp_f32_e32 v110, v110
	v_add_f32_e32 v128, v106, v128
	v_exp_f32_e32 v111, v111
	v_add_f32_e32 v128, v107, v128
	v_exp_f32_e32 v80, v80
	v_add_f32_e32 v128, v108, v128
	v_exp_f32_e32 v81, v81
	v_add_f32_e32 v128, v109, v128
	v_exp_f32_e32 v82, v82
	v_add_f32_e32 v128, v110, v128
	v_exp_f32_e32 v83, v83
	v_add_f32_e32 v128, v111, v128
	v_exp_f32_e32 v84, v84
	v_add_f32_e32 v128, v80, v128
	v_exp_f32_e32 v85, v85
	v_add_f32_e32 v128, v81, v128
	v_exp_f32_e32 v86, v86
	v_add_f32_e32 v128, v82, v128
	v_exp_f32_e32 v87, v87
	v_add_f32_e32 v128, v83, v128
	v_exp_f32_e32 v88, v88
	v_add_f32_e32 v128, v84, v128
	v_exp_f32_e32 v89, v89
	v_add_f32_e32 v128, v85, v128
	v_exp_f32_e32 v90, v90
	v_add_f32_e32 v128, v86, v128
	v_exp_f32_e32 v91, v91
	v_add_f32_e32 v128, v87, v128
	v_exp_f32_e32 v92, v92
	v_add_f32_e32 v128, v88, v128
	v_exp_f32_e32 v93, v93
	v_add_f32_e32 v128, v89, v128
	v_exp_f32_e32 v94, v94
	v_add_f32_e32 v128, v90, v128
	v_exp_f32_e32 v95, v95
	v_add_f32_e32 v128, v91, v128
	v_add_f32_e32 v128, v92, v128
	v_add_f32_e32 v128, v93, v128
	v_add_f32_e32 v128, v94, v128
	v_add_f32_e32 v128, v95, v128
	v_mov_b32_e32 v129, v128
	v_cvt_pk_bf16_f32 v162, v96, v97
	v_cvt_pk_bf16_f32 v163, v98, v99
	v_permlane32_swap_b32_e32 v128, v129
	v_add_f32_e32 v128, v128, v129
	v_add_f32_e32 v159, v159, v128
	v_cvt_pk_bf16_f32 v164, v100, v101
	v_cvt_pk_bf16_f32 v165, v102, v103
	v_cvt_pk_bf16_f32 v166, v104, v105
	v_cvt_pk_bf16_f32 v167, v106, v107
	v_cvt_pk_bf16_f32 v168, v108, v109
	v_cvt_pk_bf16_f32 v169, v110, v111
	v_cvt_pk_bf16_f32 v132, v80, v81
	v_cvt_pk_bf16_f32 v133, v82, v83
	v_cvt_pk_bf16_f32 v134, v84, v85
	v_cvt_pk_bf16_f32 v135, v86, v87
	v_cvt_pk_bf16_f32 v128, v88, v89
	v_cvt_pk_bf16_f32 v129, v90, v91
	v_cvt_pk_bf16_f32 v130, v92, v93
	v_cvt_pk_bf16_f32 v131, v94, v95
	s_waitcnt lgkmcnt(0)
	ds_read_b128 v[170:173], v232 offset:0
	ds_read_b128 v[174:177], v233 offset:0
	ds_read_b128 v[178:181], v186 offset:0
	ds_read_b128 v[182:185], v187 offset:0
	s_barrier
; #define SBAR() __builtin_amdgcn_sched_barrier(0)
; #define LWN1(a) do { if constexpr (NW == 0) LW1(0, a); else if constexpr (NW == 1) LW1(1, a); else if constexpr (NW == 2) LW1(2, a); else if constexpr (NW == 3) LW1(3, a); else if constexpr (NW == 4) LW1(4, a); else if constexpr (NW == 5) LW1(5, a); else LW1(6, a); } while (0)
; #define LWN2(a, b) do { if constexpr (NW == 0) LW2(0, a, b); else if constexpr (NW == 1) LW2(1, a, b); else if constexpr (NW == 2) LW2(2, a, b); else if constexpr (NW == 3) LW2(3, a, b); else if constexpr (NW == 4) LW2(4, a, b); else if constexpr (NW == 5) LW2(5, a, b); else LW2(6, a, b); } while (0)
; template <int DQK, bool HASQK, bool HASPV, int J> ...
;     constexpr int NQS = HASQK ? 2 * (DQK / 16) : 0, NS = NQS + (HASPV ? 16 : 0);
;     if constexpr (J < NS) {
;         constexpr int rd1 = (J + 1 < NS) ? ((J + 1 < NQS) ? 1 : 2) : 0, rd2 = (J + 2 < NS) ? ((J + 2 < NQS) ? 1 : 2) : 0, rd3 = (J + 3 < NS) ? ((J + 3 < NQS) ? 1 : 2) : 0, NW = rd1 + rd2 + rd3;
;     ...
;         if constexpr (J < NQS) { constexpr int d0 = J >> 1, h = J & 1;
;             LWN1(kf[d0][h]); SBAR();
;             if constexpr (h == 0) p0 = __builtin_amdgcn_mfma_f32_32x32x16_bf16(kf[d0][0], qr[d0], (d0 == 0) ? negm : p0, 0, 0, 0);
;             else p1 = __builtin_amdgcn_mfma_f32_32x32x16_bf16(kf[d0][1], qr[d0], (d0 == 0) ? negm : p1, 0, 0, 0);
;         } else { constexpr int q = J - NQS, g = q >> 2, d = q & 3;
;             LWN2(vf[g][2 * d], vf[g][2 * d + 1]); SBAR();
;             o[d] = __builtin_amdgcn_mfma_f32_32x32x16_bf16(pa[g], (bf16x8){vf[g][2 * d][0], vf[g][2 * d][1], vf[g][2 * d][2], vf[g][2 * d][3], vf[g][2 * d + 1][0], vf[g][2 * d + 1][1], vf[g][2 * d + 1][2], vf[g][2 * d + 1][3]}, o[d], 0, 0, 0);
;         }
;     ...
;         SBAR();
;         slot_read<DQK, HASQK, HASPV, J + 4>(kf, vf, ka_, vb_);
;         SBAR();
;         slot_run<DQK, HASQK, HASPV, J + 1>(kf, vf, ka_, vb_, qr, p0, p1, negm, o, pa);
; template <int DQK, bool HASQK, bool HASPV>
; __device__ __forceinline__ void seg_m2(const int (&ka_)[4], int vb_, const bf16x8* qr, f32x16& p0, f32x16& p1, const float nm, f32x16 (&o)[4], bf16x8 pa0, bf16x8 pa1, bf16x8 pa2, bf16x8 pa3) {
;     ...
;     f32x16 negm;
; #pragma unroll
;     for (int r = 0; r < 16; ++r) negm[r] = nm;
;     asm volatile("" : "+v"(negm));
	s_waitcnt lgkmcnt(3)
	v_mfma_f32_32x32x16_bf16 v[96:111], v[170:173], v[112:115], v[200:215]
	v_xor_b32_e32 v80, 0x80000000, v158
	v_mov_b32_e32 v81, v80
	v_mov_b32_e32 v82, v80
	v_mov_b32_e32 v83, v80
	v_mov_b32_e32 v84, v80
	ds_read_b128 v[170:173], v232 offset:4096
	s_waitcnt lgkmcnt(3)
	v_mfma_f32_32x32x16_bf16 v[96:111], v[174:177], v[116:119], v[96:111]
	v_mov_b32_e32 v85, v80
	v_mov_b32_e32 v86, v80
	v_mov_b32_e32 v87, v80
	v_mov_b32_e32 v88, v80
	ds_read_b128 v[174:177], v233 offset:4096
	s_waitcnt lgkmcnt(3)
	v_mfma_f32_32x32x16_bf16 v[96:111], v[178:181], v[120:123], v[96:111]
	v_mov_b32_e32 v89, v80
	v_mov_b32_e32 v90, v80
	v_mov_b32_e32 v91, v80
	v_mov_b32_e32 v92, v80
	ds_read_b128 v[178:181], v186 offset:4096
	s_waitcnt lgkmcnt(3)
	v_mfma_f32_32x32x16_bf16 v[96:111], v[182:185], v[124:127], v[96:111]
	v_mov_b32_e32 v93, v80
	v_mov_b32_e32 v94, v80
	v_mov_b32_e32 v95, v80
	ds_read_b128 v[182:185], v187 offset:4096
	s_waitcnt lgkmcnt(3)
	v_mfma_f32_32x32x16_bf16 v[80:95], v[170:173], v[112:115], v[80:95]
	ds_read_b64_tr_b16 v[170:171], v188 offset:0
	ds_read_b64_tr_b16 v[172:173], v188 offset:2048
	s_waitcnt lgkmcnt(4)
	v_mfma_f32_32x32x16_bf16 v[80:95], v[174:177], v[116:119], v[80:95]
	ds_read_b64_tr_b16 v[174:175], v188 offset:512
	ds_read_b64_tr_b16 v[176:177], v188 offset:2560
	s_waitcnt lgkmcnt(5)
	v_mfma_f32_32x32x16_bf16 v[80:95], v[178:181], v[120:123], v[80:95]
	ds_read_b64_tr_b16 v[178:179], v188 offset:1024
	ds_read_b64_tr_b16 v[180:181], v188 offset:3072
	s_waitcnt lgkmcnt(6)
	v_mfma_f32_32x32x16_bf16 v[80:95], v[182:185], v[124:127], v[80:95]
	ds_read_b64_tr_b16 v[182:183], v188 offset:1536
	ds_read_b64_tr_b16 v[184:185], v188 offset:3584
	s_waitcnt lgkmcnt(6)
	v_mfma_f32_32x32x16_bf16 v[64:79], v[162:165], v[170:173], v[64:79]
	ds_read_b64_tr_b16 v[170:171], v188 offset:4096
	ds_read_b64_tr_b16 v[172:173], v188 offset:6144
	s_waitcnt lgkmcnt(6)
	v_mfma_f32_32x32x16_bf16 v[48:63], v[162:165], v[174:177], v[48:63]
	ds_read_b64_tr_b16 v[174:175], v188 offset:4608
	ds_read_b64_tr_b16 v[176:177], v188 offset:6656
	s_waitcnt lgkmcnt(6)
	v_mfma_f32_32x32x16_bf16 v[32:47], v[162:165], v[178:181], v[32:47]
	ds_read_b64_tr_b16 v[178:179], v188 offset:5120
	ds_read_b64_tr_b16 v[180:181], v188 offset:7168
	s_waitcnt lgkmcnt(6)
	v_mfma_f32_32x32x16_bf16 v[16:31], v[162:165], v[182:185], v[16:31]
	ds_read_b64_tr_b16 v[182:183], v188 offset:5632
	ds_read_b64_tr_b16 v[184:185], v188 offset:7680
	s_waitcnt lgkmcnt(6)
	v_mfma_f32_32x32x16_bf16 v[64:79], v[166:169], v[170:173], v[64:79]
	ds_read_b64_tr_b16 v[170:171], v188 offset:8192
	ds_read_b64_tr_b16 v[172:173], v188 offset:10240
	s_waitcnt lgkmcnt(6)
	v_mfma_f32_32x32x16_bf16 v[48:63], v[166:169], v[174:177], v[48:63]
	ds_read_b64_tr_b16 v[174:175], v188 offset:8704
	ds_read_b64_tr_b16 v[176:177], v188 offset:10752
	s_waitcnt lgkmcnt(6)
	v_mfma_f32_32x32x16_bf16 v[32:47], v[166:169], v[178:181], v[32:47]
	ds_read_b64_tr_b16 v[178:179], v188 offset:9216
	ds_read_b64_tr_b16 v[180:181], v188 offset:11264
	s_waitcnt lgkmcnt(6)
	v_mfma_f32_32x32x16_bf16 v[16:31], v[166:169], v[182:185], v[16:31]
	ds_read_b64_tr_b16 v[182:183], v188 offset:9728
	ds_read_b64_tr_b16 v[184:185], v188 offset:11776
	s_waitcnt lgkmcnt(6)
	v_mfma_f32_32x32x16_bf16 v[64:79], v[132:135], v[170:173], v[64:79]
	ds_read_b64_tr_b16 v[170:171], v188 offset:12288
	ds_read_b64_tr_b16 v[172:173], v188 offset:14336
	s_waitcnt lgkmcnt(6)
	v_mfma_f32_32x32x16_bf16 v[48:63], v[132:135], v[174:177], v[48:63]
	ds_read_b64_tr_b16 v[174:175], v188 offset:12800
	ds_read_b64_tr_b16 v[176:177], v188 offset:14848
	s_waitcnt lgkmcnt(6)
	v_mfma_f32_32x32x16_bf16 v[32:47], v[132:135], v[178:181], v[32:47]
	ds_read_b64_tr_b16 v[178:179], v188 offset:13312
	ds_read_b64_tr_b16 v[180:181], v188 offset:15360
	s_waitcnt lgkmcnt(6)
	v_mfma_f32_32x32x16_bf16 v[16:31], v[132:135], v[182:185], v[16:31]
	ds_read_b64_tr_b16 v[182:183], v188 offset:13824
	ds_read_b64_tr_b16 v[184:185], v188 offset:15872
	s_waitcnt lgkmcnt(6)
	v_mfma_f32_32x32x16_bf16 v[64:79], v[128:131], v[170:173], v[64:79]
	s_waitcnt lgkmcnt(4)
	v_mfma_f32_32x32x16_bf16 v[48:63], v[128:131], v[174:177], v[48:63]
	s_waitcnt lgkmcnt(2)
	v_mfma_f32_32x32x16_bf16 v[32:47], v[128:131], v[178:181], v[32:47]
	s_waitcnt lgkmcnt(0)
	v_mfma_f32_32x32x16_bf16 v[16:31], v[128:131], v[182:185], v[16:31]
	v_lshl_add_u64 v[144:145], v[144:145], 0, s[28:29]
	v_lshl_add_u64 v[146:147], v[146:147], 0, s[28:29]
	v_lshl_add_u64 v[148:149], v[148:149], 0, s[28:29]
	s_add_i32 s46, s86, 1
	s_cmp_lg_u32 s86, 2
	s_cselect_b32 s46, s46, 0
	s_lshl_b32 s47, s46, 13
	s_lshl_b32 s46, s86, 14
	v_add_u32_e32 v188, s46, v157
	v_add_u32_e32 v232, s47, v141
	v_add_u32_e32 v233, s47, v143
	v_add_u32_e32 v186, s47, v160
	v_add_u32_e32 v187, s47, v161
	s_waitcnt vmcnt(0)
	s_add_u32 s44, s44, 0x10000
	s_waitcnt lgkmcnt(0)
	s_barrier
	s_addc_u32 s45, s45, 0
	s_cmp_eq_u32 s44, 0x7f0000
	s_cbranch_scc1 .LBB0_662
